# baseline (speedup 1.0000x reference)
_Z10qkv_kernelPKfS0_S0_PKdPKtS0_PhPfS6_:
	s_load_dwordx2 s[8:9], s[0:1], 0x0
	s_load_dwordx4 s[4:7], s[0:1], 0x18
	s_load_dwordx4 s[20:23], s[0:1], 0x8
	v_lshrrev_b32_e32 v1, 6, v0
	v_and_b32_e32 v146, 63, v0
	v_lshlrev_b32_e32 v134, 14, v1
	v_mov_b32_e32 v135, 0
	s_waitcnt lgkmcnt(0)
	v_lshrrev_b32_e32 v188, 6, v0
	v_and_b32_e32 v189, 31, v0
	v_lshl_add_u32 v188, v188, 5, v189
	v_lshlrev_b32_e32 v188, 2, v188
	global_load_dword v190, v188, s[20:21]
	global_load_dword v191, v188, s[22:23]
	v_lshl_add_u64 v[2:3], s[6:7], 0, v[134:135]
	v_lshlrev_b32_e32 v134, 4, v146
	s_ashr_i32 s6, s2, 6
	v_lshl_add_u64 v[132:133], v[2:3], 0, v[134:135]
	v_lshl_or_b32 v2, s6, 3, v1
	v_ashrrev_i32_e32 v3, 31, v2
	v_lshlrev_b64 v[2:3], 10, v[2:3]
	v_lshl_add_u64 v[2:3], s[4:5], 0, v[2:3]
	v_lshl_add_u64 v[2:3], v[2:3], 0, v[134:135]
	global_load_dwordx4 v[98:101], v[2:3], off
	s_movk_i32 s7, 0x1000
	v_add_co_u32_e32 v2, vcc, s7, v132
	s_lshl_b32 s3, s2, 6
	s_nop 0
	v_addc_co_u32_e32 v3, vcc, 0, v133, vcc
	s_movk_i32 s4, 0x2000
	v_add_co_u32_e32 v4, vcc, s4, v132
	s_and_b32 s3, s3, 0xfc0
	s_nop 0
	v_addc_co_u32_e32 v5, vcc, 0, v133, vcc
	s_movk_i32 s4, 0x3000
	s_ashr_i32 s7, s6, 31
	s_lshl_b32 s16, s3, 2
	v_add_co_u32_e32 v4, vcc, s4, v132
	v_and_b32_e32 v106, 7, v0
	s_add_u32 s4, s8, s16
	v_addc_co_u32_e32 v5, vcc, 0, v133, vcc
	s_addc_u32 s5, s9, 0
	v_lshlrev_b32_e32 v2, 5, v106
	v_mov_b32_e32 v3, v135
	v_lshrrev_b32_e32 v107, 3, v0
	v_lshl_add_u64 v[2:3], s[4:5], 0, v[2:3]
	s_lshl_b64 s[4:5], s[6:7], 22
	v_lshl_or_b32 v4, v107, 14, s4
	v_mov_b32_e32 v5, s5
	v_lshl_add_u64 v[2:3], v[2:3], 0, v[4:5]
	s_mov_b64 s[4:5], 0x100000
	v_lshl_add_u64 v[4:5], v[2:3], 0, s[4:5]
	s_mov_b32 s4, 0x100000
	v_add_co_u32_e32 v6, vcc, s4, v2
	s_mov_b64 s[4:5], 0x200000
	s_nop 0
	v_addc_co_u32_e32 v7, vcc, 0, v3, vcc
	global_load_dwordx4 v[26:29], v[2:3], off offset:16
	global_load_dwordx4 v[30:33], v[2:3], off
	global_load_dwordx4 v[22:25], v[6:7], off
	global_load_dwordx4 v[18:21], v[4:5], off offset:16
	v_lshl_add_u64 v[4:5], v[2:3], 0, s[4:5]
	s_mov_b32 s4, 0x200000
	v_add_co_u32_e32 v6, vcc, s4, v2
	s_mov_b64 s[4:5], 0x300000
	s_nop 0
	v_addc_co_u32_e32 v7, vcc, 0, v3, vcc
	v_lshl_add_u64 v[102:103], v[2:3], 0, s[4:5]
	s_mov_b32 s4, 0x300000
	v_add_co_u32_e32 v104, vcc, s4, v2
	global_load_dwordx4 v[14:17], v[6:7], off
	global_load_dwordx4 v[10:13], v[4:5], off offset:16
	v_addc_co_u32_e32 v105, vcc, 0, v3, vcc
	global_load_dwordx4 v[6:9], v[104:105], off
	global_load_dwordx4 v[2:5], v[102:103], off offset:16
	s_mov_b64 s[24:25], 0x1000
	s_mov_b64 s[26:27], 0x2000
	s_mov_b64 s[28:29], 0x3000
	v_lshl_add_u64 v[182:183], v[132:133], 0, s[24:25]
	v_lshl_add_u64 v[184:185], v[132:133], 0, s[26:27]
	v_lshl_add_u64 v[186:187], v[132:133], 0, s[28:29]
	global_load_dwordx4 v[94:97], v[132:133], off
	global_load_dwordx4 v[86:89], v[132:133], off offset:1024
	global_load_dwordx4 v[54:57], v[132:133], off offset:2048
	global_load_dwordx4 v[42:45], v[132:133], off offset:3072
	global_load_dwordx4 v[78:81], v[182:183], off offset:1024
	global_load_dwordx4 v[82:85], v[182:183], off offset:2048
	global_load_dwordx4 v[74:77], v[182:183], off offset:3072
	global_load_dwordx4 v[90:93], v[184:185], off offset:-4096
	global_load_dwordx4 v[66:69], v[184:185], off
	global_load_dwordx4 v[70:73], v[184:185], off offset:1024
	global_load_dwordx4 v[62:65], v[184:185], off offset:2048
	global_load_dwordx4 v[58:61], v[184:185], off offset:3072
	global_load_dwordx4 v[50:53], v[186:187], off
	global_load_dwordx4 v[46:49], v[186:187], off offset:1024
	global_load_dwordx4 v[38:41], v[186:187], off offset:2048
	global_load_dwordx4 v[34:37], v[186:187], off offset:3072
	v_mbcnt_lo_u32_b32 v102, -1, 0
	v_mbcnt_hi_u32_b32 v108, -1, v102
	v_and_b32_e32 v102, 64, v108
	v_add_u32_e32 v109, 64, v102
	v_xor_b32_e32 v102, 32, v108
	v_cmp_lt_i32_e32 vcc, v102, v109
	s_load_dwordx2 s[8:9], s[0:1], 0x28
	v_cmp_lt_u32_e64 s[4:5], 31, v146
	v_cndmask_b32_e32 v102, v108, v102, vcc
	v_lshlrev_b32_e32 v105, 2, v102
	v_lshlrev_b32_e32 v130, 5, v1
	s_waitcnt vmcnt(24)
	ds_bpermute_b32 v102, v105, v98
	ds_bpermute_b32 v103, v105, v99
	ds_bpermute_b32 v104, v105, v100
	ds_bpermute_b32 v105, v105, v101
	s_waitcnt lgkmcnt(0)
	v_add_f64 v[98:99], v[98:99], v[102:103]
	v_xor_b32_e32 v102, 16, v108
	v_cmp_lt_i32_e32 vcc, v102, v109
	v_add_f64 v[100:101], v[100:101], v[104:105]
	s_nop 0
	v_cndmask_b32_e32 v102, v108, v102, vcc
	v_lshlrev_b32_e32 v141, 2, v102
	ds_bpermute_b32 v102, v141, v98
	ds_bpermute_b32 v103, v141, v99
	ds_bpermute_b32 v104, v141, v100
	ds_bpermute_b32 v105, v141, v101
	s_waitcnt lgkmcnt(2)
	v_add_f64 v[98:99], v[98:99], v[102:103]
	v_xor_b32_e32 v102, 8, v108
	v_cmp_lt_i32_e32 vcc, v102, v109
	s_waitcnt lgkmcnt(0)
	v_add_f64 v[100:101], v[100:101], v[104:105]
	v_cndmask_b32_e32 v102, v108, v102, vcc
	v_lshlrev_b32_e32 v142, 2, v102
	ds_bpermute_b32 v102, v142, v98
	ds_bpermute_b32 v103, v142, v99
	ds_bpermute_b32 v104, v142, v100
	ds_bpermute_b32 v105, v142, v101
	s_waitcnt lgkmcnt(2)
	v_add_f64 v[98:99], v[98:99], v[102:103]
	v_xor_b32_e32 v102, 4, v108
	v_cmp_lt_i32_e32 vcc, v102, v109
	s_waitcnt lgkmcnt(0)
	v_add_f64 v[100:101], v[100:101], v[104:105]
	v_cndmask_b32_e32 v102, v108, v102, vcc
	v_lshlrev_b32_e32 v143, 2, v102
	ds_bpermute_b32 v102, v143, v98
	ds_bpermute_b32 v103, v143, v99
	ds_bpermute_b32 v104, v143, v100
	ds_bpermute_b32 v105, v143, v101
	s_waitcnt lgkmcnt(2)
	v_add_f64 v[98:99], v[98:99], v[102:103]
	v_xor_b32_e32 v102, 2, v108
	v_cmp_lt_i32_e32 vcc, v102, v109
	s_waitcnt lgkmcnt(0)
	v_add_f64 v[100:101], v[100:101], v[104:105]
	v_cndmask_b32_e32 v102, v108, v102, vcc
	v_lshlrev_b32_e32 v144, 2, v102
	ds_bpermute_b32 v102, v144, v98
	ds_bpermute_b32 v103, v144, v99
	ds_bpermute_b32 v104, v144, v100
	ds_bpermute_b32 v105, v144, v101
	s_waitcnt lgkmcnt(2)
	v_add_f64 v[98:99], v[98:99], v[102:103]
	v_xor_b32_e32 v102, 1, v108
	v_cmp_lt_i32_e32 vcc, v102, v109
	s_waitcnt lgkmcnt(0)
	v_add_f64 v[100:101], v[100:101], v[104:105]
	v_cndmask_b32_e32 v102, v108, v102, vcc
	v_lshlrev_b32_e32 v145, 2, v102
	ds_bpermute_b32 v102, v145, v98
	ds_bpermute_b32 v103, v145, v99
	ds_bpermute_b32 v104, v145, v100
	ds_bpermute_b32 v105, v145, v101
	v_cmp_gt_u32_e32 vcc, 32, v146
	s_and_saveexec_b64 s[10:11], s[4:5]
	s_xor_b64 s[4:5], exec, s[10:11]
	v_lshlrev_b32_e32 v130, 5, v1
	s_or_saveexec_b64 s[10:11], s[4:5]
	s_load_dwordx2 s[14:15], s[0:1], 0x38
	s_xor_b64 exec, exec, s[10:11]
	s_cbranch_execz .LBB1_4
	s_load_dwordx4 s[20:23], s[0:1], 0x8
	v_or_b32_e32 v108, v130, v146
	v_lshlrev_b32_e32 v108, 2, v108
	s_waitcnt lgkmcnt(0)
	v_add_f64 v[98:99], v[98:99], v[102:103]
	s_movk_i32 s12, 0xffef
	s_mov_b32 s4, 0
	v_ldexp_f64 v[98:99], v[98:99], s12
	v_add_f64 v[100:101], v[100:101], v[104:105]
	s_mov_b32 s5, 0x3ee00000
	v_mul_f64 v[102:103], v[98:99], v[98:99]
	v_fma_f64 v[100:101], v[100:101], s[4:5], -v[102:103]
	v_cvt_f32_f64_e32 v100, v[100:101]
	s_mov_b32 s13, 0x800000
	v_add_f32_e32 v100, 0x3727c5ac, v100
	v_mul_f32_e32 v101, 0x4b800000, v100
	v_cmp_gt_f32_e64 s[4:5], s13, v100
	v_cvt_f32_f64_e32 v98, v[98:99]
	s_nop 0
	v_cndmask_b32_e64 v100, v100, v101, s[4:5]
	v_rsq_f32_e32 v100, v100
	v_add_u32_e32 v101, 0, v108
	v_mul_f32_e32 v102, 0x45800000, v100
	v_cndmask_b32_e64 v100, v100, v102, s[4:5]
	v_mul_f32_e32 v100, v100, v190
	v_fma_f32 v98, -v100, v98, v191
	ds_write2st64_b32 v101, v100, v98 offset0:128 offset1:132
.LBB1_4:
	s_or_b64 exec, exec, s[10:11]
	s_waitcnt lgkmcnt(0)
	v_lshrrev_b32_e32 v103, 4, v0
	v_bfe_u32 v104, v0, 3, 2
	v_lshlrev_b32_e32 v102, 4, v0
	v_and_or_b32 v103, v103, 4, v104
	v_lshl_add_u32 v105, v107, 2, 0
	v_lshlrev_b32_e32 v103, 6, v103
	v_and_b32_e32 v102, 48, v102
	s_barrier
	ds_read2st64_b32 v[98:99], v105 offset0:128 offset1:129
	ds_read2st64_b32 v[100:101], v105 offset0:132 offset1:133
	v_add3_u32 v109, 0, v103, v102
	ds_read2st64_b32 v[102:103], v105 offset0:134 offset1:135
	ds_read2st64_b32 v[104:105], v105 offset0:130 offset1:131
	s_movk_i32 s4, 0x70
	v_lshrrev_b32_e32 v108, 5, v146
	s_waitcnt vmcnt(21) lgkmcnt(2)
	v_fma_f32 v22, v22, v99, v101
	v_fma_f32 v23, v23, v99, v101
	s_waitcnt vmcnt(19) lgkmcnt(0)
	v_fma_f32 v14, v14, v104, v102
	v_fma_f32 v15, v15, v104, v102
	v_cvt_pk_bf16_f32 v22, v22, v23
	v_fma_f32 v23, v24, v99, v101
	v_fma_f32 v24, v25, v99, v101
	v_fma_f32 v18, v18, v99, v101
	v_fma_f32 v19, v19, v99, v101
	v_cvt_pk_bf16_f32 v14, v14, v15
	v_fma_f32 v15, v16, v104, v102
	v_fma_f32 v16, v17, v104, v102
	s_waitcnt vmcnt(18)
	v_fma_f32 v10, v10, v104, v102
	v_fma_f32 v11, v11, v104, v102
	s_waitcnt vmcnt(17)
	v_fma_f32 v6, v6, v105, v103
	v_fma_f32 v7, v7, v105, v103
	v_fma_f32 v30, v30, v98, v100
	v_fma_f32 v31, v31, v98, v100
	v_fma_f32 v32, v32, v98, v100
	v_fma_f32 v33, v33, v98, v100
	v_fma_f32 v26, v26, v98, v100
	v_fma_f32 v27, v27, v98, v100
	v_cvt_pk_bf16_f32 v23, v23, v24
	v_cvt_pk_bf16_f32 v24, v18, v19
	v_fma_f32 v18, v20, v99, v101
	v_fmac_f32_e32 v101, v21, v99
	v_cvt_pk_bf16_f32 v15, v15, v16
	v_cvt_pk_bf16_f32 v16, v10, v11
	v_fma_f32 v10, v12, v104, v102
	v_fma_f32 v11, v13, v104, v102
	v_cvt_pk_bf16_f32 v6, v6, v7
	v_fma_f32 v7, v8, v105, v103
	v_fma_f32 v8, v9, v105, v103
	s_waitcnt vmcnt(16)
	v_fma_f32 v2, v2, v105, v103
	v_fma_f32 v3, v3, v105, v103
	v_cvt_pk_bf16_f32 v30, v30, v31
	v_cvt_pk_bf16_f32 v31, v32, v33
	v_cvt_pk_bf16_f32 v32, v26, v27
	v_fma_f32 v26, v28, v98, v100
	v_fma_f32 v27, v29, v98, v100
	v_cvt_pk_bf16_f32 v25, v18, v101
	v_bitop3_b32 v18, v107, s4, 64 bitop3:0xc8
	v_cvt_pk_bf16_f32 v17, v10, v11
	s_movk_i32 s4, 0xb0
	v_mov_b32_e32 v10, 0x80
	v_cvt_pk_bf16_f32 v7, v7, v8
	v_cvt_pk_bf16_f32 v8, v2, v3
	v_fma_f32 v2, v4, v105, v103
	v_fmac_f32_e32 v103, v5, v105
	v_cvt_pk_bf16_f32 v33, v26, v27
	v_lshlrev_b32_e32 v27, 1, v107
	v_bitop3_b32 v10, v107, s4, v10 bitop3:0xc8
	v_cvt_pk_bf16_f32 v9, v2, v103
	s_movk_i32 s4, 0xf0
	v_mov_b32_e32 v2, 0xc0
	v_and_b32_e32 v26, 48, v107
	v_and_b32_e32 v27, 8, v27
	v_bitop3_b32 v2, v107, s4, v2 bitop3:0xc8
	v_or3_b32 v26, v26, v27, v106
	v_or3_b32 v18, v18, v27, v106
	v_or3_b32 v10, v10, v27, v106
	v_or3_b32 v2, v2, v27, v106
	v_lshlrev_b32_e32 v26, 7, v26
	v_lshlrev_b32_e32 v18, 7, v18
	v_lshlrev_b32_e32 v10, 7, v10
	v_lshlrev_b32_e32 v2, 7, v2
	v_and_b32_e32 v26, 0x1e00, v26
	v_and_b32_e32 v18, 0x3e00, v18
	v_and_b32_e32 v10, 0x5e00, v10
	v_and_b32_e32 v2, 0x7e00, v2
	v_add_u32_e32 v26, v109, v26
	v_add_u32_e32 v18, v109, v18
	v_add_u32_e32 v10, v109, v10
	v_add_u32_e32 v2, v109, v2
	v_mov_b32_e32 v131, 0
	ds_write_b128 v26, v[30:33]
	ds_write_b128 v18, v[22:25]
	ds_write_b128 v10, v[14:17]
	ds_write_b128 v2, v[6:9]
	v_lshl_add_u64 v[2:3], v[130:131], 2, s[8:9]
	v_lshlrev_b32_e32 v136, 4, v108
	v_mov_b32_e32 v137, v131
	v_lshl_add_u64 v[138:139], v[2:3], 0, v[136:137]
	s_waitcnt lgkmcnt(0)
	s_barrier
	global_load_dwordx4 v[2:5], v[138:139], off
	global_load_dwordx4 v[6:9], v[138:139], off offset:32
	global_load_dwordx4 v[10:13], v[138:139], off offset:64
	global_load_dwordx4 v[14:17], v[138:139], off offset:96
	v_lshlrev_b32_e32 v18, 3, v146
	v_and_b32_e32 v19, 24, v18
	v_and_b32_e32 v20, 0xc0, v134
	v_lshlrev_b32_e32 v21, 1, v0
	v_and_b32_e32 v21, 32, v21
	v_and_b32_e32 v18, 0x100, v18
	v_add3_u32 v19, 0, v19, v20
	v_add3_u32 v140, v19, v21, v18
	ds_read_b64_tr_b16 v[98:99], v140
	ds_read_b64_tr_b16 v[100:101], v140 offset:1024
	ds_read_b64_tr_b16 v[104:105], v140 offset:1536
	ds_read_b64_tr_b16 v[102:103], v140 offset:512
	s_waitcnt vmcnt(0) lgkmcnt(2)
	v_mfma_f32_32x32x16_bf16 v[18:33], v[94:97], v[98:101], v[2:17]
	ds_read_b64_tr_b16 v[98:99], v140 offset:2048
	ds_read_b64_tr_b16 v[100:101], v140 offset:3072
	ds_read_b64_tr_b16 v[108:109], v140 offset:3584
	ds_read_b64_tr_b16 v[106:107], v140 offset:2560
	s_mov_b32 s4, 0x20000
	v_and_b32_e32 v137, 31, v0
	s_waitcnt lgkmcnt(2)
	v_mfma_f32_32x32x16_bf16 v[18:33], v[86:89], v[98:101], v[18:33]
	ds_read_b64_tr_b16 v[98:99], v140 offset:4096
	ds_read_b64_tr_b16 v[100:101], v140 offset:5120
	ds_read_b64_tr_b16 v[112:113], v140 offset:5632
	ds_read_b64_tr_b16 v[110:111], v140 offset:4608
	s_waitcnt lgkmcnt(2)
	v_mfma_f32_32x32x16_bf16 v[18:33], v[54:57], v[98:101], v[18:33]
	v_mfma_f32_32x32x16_bf16 v[2:17], v[94:97], v[102:105], v[2:17]
	ds_read_b64_tr_b16 v[94:95], v140 offset:6144
	ds_read_b64_tr_b16 v[96:97], v140 offset:7168
	ds_read_b64_tr_b16 v[100:101], v140 offset:7680
	ds_read_b64_tr_b16 v[98:99], v140 offset:6656
	s_waitcnt lgkmcnt(2)
	v_mfma_f32_32x32x16_bf16 v[18:33], v[42:45], v[94:97], v[18:33]
	ds_read_b64_tr_b16 v[94:95], v140 offset:8192
	ds_read_b64_tr_b16 v[96:97], v140 offset:9216
	ds_read_b64_tr_b16 v[104:105], v140 offset:9728
	ds_read_b64_tr_b16 v[102:103], v140 offset:8704
	v_mfma_f32_32x32x16_bf16 v[2:17], v[86:89], v[106:109], v[2:17]
	s_waitcnt lgkmcnt(2)
	v_mfma_f32_32x32x16_bf16 v[18:33], v[90:93], v[94:97], v[18:33]
	ds_read_b64_tr_b16 v[86:87], v140 offset:10240
	ds_read_b64_tr_b16 v[88:89], v140 offset:11264
	ds_read_b64_tr_b16 v[96:97], v140 offset:11776
	ds_read_b64_tr_b16 v[94:95], v140 offset:10752
	v_mfma_f32_32x32x16_bf16 v[2:17], v[54:57], v[110:113], v[2:17]
	s_waitcnt lgkmcnt(2)
	v_mfma_f32_32x32x16_bf16 v[18:33], v[78:81], v[86:89], v[18:33]
	ds_read_b64_tr_b16 v[86:87], v140 offset:12288
	ds_read_b64_tr_b16 v[88:89], v140 offset:13312
	ds_read_b64_tr_b16 v[108:109], v140 offset:13824
	ds_read_b64_tr_b16 v[106:107], v140 offset:12800
	v_mfma_f32_32x32x16_bf16 v[2:17], v[42:45], v[98:101], v[2:17]
	s_waitcnt lgkmcnt(2)
	v_mfma_f32_32x32x16_bf16 v[18:33], v[82:85], v[86:89], v[18:33]
	ds_read_b64_tr_b16 v[54:55], v140 offset:14336
	ds_read_b64_tr_b16 v[56:57], v140 offset:15360
	ds_read_b64_tr_b16 v[88:89], v140 offset:15872
	ds_read_b64_tr_b16 v[86:87], v140 offset:14848
	v_mfma_f32_32x32x16_bf16 v[2:17], v[90:93], v[102:105], v[2:17]
	s_waitcnt lgkmcnt(2)
	v_mfma_f32_32x32x16_bf16 v[18:33], v[74:77], v[54:57], v[18:33]
	ds_read_b64_tr_b16 v[54:55], v140 offset:16384
	ds_read_b64_tr_b16 v[56:57], v140 offset:17408
	ds_read_b64_tr_b16 v[112:113], v140 offset:17920
	ds_read_b64_tr_b16 v[110:111], v140 offset:16896
	v_mfma_f32_32x32x16_bf16 v[2:17], v[78:81], v[94:97], v[2:17]
	s_waitcnt lgkmcnt(2)
	v_mfma_f32_32x32x16_bf16 v[18:33], v[66:69], v[54:57], v[18:33]
	ds_read_b64_tr_b16 v[42:43], v140 offset:18432
	ds_read_b64_tr_b16 v[44:45], v140 offset:19456
	ds_read_b64_tr_b16 v[56:57], v140 offset:19968
	ds_read_b64_tr_b16 v[54:55], v140 offset:18944
	v_mfma_f32_32x32x16_bf16 v[2:17], v[82:85], v[106:109], v[2:17]
	s_waitcnt lgkmcnt(2)
	v_mfma_f32_32x32x16_bf16 v[18:33], v[70:73], v[42:45], v[18:33]
	ds_read_b64_tr_b16 v[42:43], v140 offset:20480
	ds_read_b64_tr_b16 v[44:45], v140 offset:21504
	ds_read_b64_tr_b16 v[80:81], v140 offset:22016
	ds_read_b64_tr_b16 v[78:79], v140 offset:20992
	v_mfma_f32_32x32x16_bf16 v[2:17], v[74:77], v[86:89], v[2:17]
	s_waitcnt lgkmcnt(2)
	v_mfma_f32_32x32x16_bf16 v[18:33], v[62:65], v[42:45], v[18:33]
	ds_read_b64_tr_b16 v[42:43], v140 offset:22528
	ds_read_b64_tr_b16 v[44:45], v140 offset:23552
	ds_read_b64_tr_b16 v[76:77], v140 offset:24064
	ds_read_b64_tr_b16 v[74:75], v140 offset:23040
	v_mfma_f32_32x32x16_bf16 v[2:17], v[66:69], v[110:113], v[2:17]
	s_waitcnt lgkmcnt(2)
	v_mfma_f32_32x32x16_bf16 v[18:33], v[58:61], v[42:45], v[18:33]
	v_mfma_f32_32x32x16_bf16 v[2:17], v[70:73], v[54:57], v[2:17]
	ds_read_b64_tr_b16 v[42:43], v140 offset:24576
	ds_read_b64_tr_b16 v[44:45], v140 offset:25600
	ds_read_b64_tr_b16 v[56:57], v140 offset:26112
	ds_read_b64_tr_b16 v[54:55], v140 offset:25088
	s_waitcnt lgkmcnt(2)
	v_mfma_f32_32x32x16_bf16 v[18:33], v[50:53], v[42:45], v[18:33]
	ds_read_b64_tr_b16 v[42:43], v140 offset:26624
	ds_read_b64_tr_b16 v[44:45], v140 offset:27648
	ds_read_b64_tr_b16 v[68:69], v140 offset:28160
	ds_read_b64_tr_b16 v[66:67], v140 offset:27136
	v_mfma_f32_32x32x16_bf16 v[2:17], v[62:65], v[78:81], v[2:17]
	s_waitcnt lgkmcnt(2)
	v_mfma_f32_32x32x16_bf16 v[18:33], v[46:49], v[42:45], v[18:33]
	ds_read_b64_tr_b16 v[42:43], v140 offset:28672
	ds_read_b64_tr_b16 v[44:45], v140 offset:29696
	ds_read_b64_tr_b16 v[150:151], v140 offset:30208
	ds_read_b64_tr_b16 v[148:149], v140 offset:29184
	v_mfma_f32_32x32x16_bf16 v[2:17], v[58:61], v[74:77], v[2:17]
	s_waitcnt lgkmcnt(2)
	v_mfma_f32_32x32x16_bf16 v[18:33], v[38:41], v[42:45], v[18:33]
	v_add_co_u32_e64 v42, s[4:5], s4, v132
	s_nop 1
	v_addc_co_u32_e64 v43, s[4:5], 0, v133, s[4:5]
	s_mov_b32 s4, 0x21000
	s_nop 0
	v_add_co_u32_e64 v44, s[4:5], s4, v132
	v_mfma_f32_32x32x16_bf16 v[2:17], v[50:53], v[54:57], v[2:17]
	s_nop 0
	v_addc_co_u32_e64 v45, s[4:5], 0, v133, s[4:5]
	s_mov_b32 s4, 0x22000
	s_nop 0
	v_add_co_u32_e64 v50, s[4:5], s4, v132
	global_load_dwordx4 v[122:125], v[42:43], off offset:1024
	global_load_dwordx4 v[114:117], v[42:43], off offset:2048
	global_load_dwordx4 v[126:129], v[44:45], off offset:-4096
	global_load_dwordx4 v[110:113], v[44:45], off
	global_load_dwordx4 v[106:109], v[44:45], off offset:1024
	global_load_dwordx4 v[102:105], v[44:45], off offset:2048
	v_addc_co_u32_e64 v51, s[4:5], 0, v133, s[4:5]
	s_mov_b32 s4, 0x23000
	s_nop 0
	v_add_co_u32_e64 v52, s[4:5], s4, v132
	v_mfma_f32_32x32x16_bf16 v[2:17], v[46:49], v[66:69], v[2:17]
	s_nop 0
	v_addc_co_u32_e64 v53, s[4:5], 0, v133, s[4:5]
	global_load_dwordx4 v[98:101], v[44:45], off offset:3072
	global_load_dwordx4 v[94:97], v[52:53], off offset:-4096
	global_load_dwordx4 v[118:121], v[42:43], off offset:3072
	global_load_dwordx4 v[90:93], v[50:51], off offset:1024
	global_load_dwordx4 v[86:89], v[50:51], off offset:2048
	global_load_dwordx4 v[82:85], v[50:51], off offset:3072
	global_load_dwordx4 v[70:73], v[52:53], off
	global_load_dwordx4 v[66:69], v[52:53], off offset:1024
	global_load_dwordx4 v[74:77], v[52:53], off offset:2048
	global_load_dwordx4 v[78:81], v[52:53], off offset:3072
	s_waitcnt lgkmcnt(0)
	v_mfma_f32_32x32x16_bf16 v[2:17], v[38:41], v[148:151], v[2:17]
	ds_read_b64_tr_b16 v[38:39], v140 offset:30720
	ds_read_b64_tr_b16 v[40:41], v140 offset:31744
	ds_read_b64_tr_b16 v[44:45], v140 offset:32256
	ds_read_b64_tr_b16 v[42:43], v140 offset:31232
	s_waitcnt lgkmcnt(0)
	s_barrier
	v_mfma_f32_32x32x16_bf16 v[18:33], v[34:37], v[38:41], v[18:33]
	v_lshl_add_u32 v38, v137, 2, 0
	v_mfma_f32_32x32x16_bf16 v[2:17], v[34:37], v[42:45], v[2:17]
	s_nop 9
	v_max3_f32 v39, |v18|, 0, |v19|
	v_max3_f32 v39, v39, |v20|, |v21|
	v_max3_f32 v39, v39, |v22|, |v23|
	v_max3_f32 v39, v39, |v24|, |v25|
	v_max3_f32 v39, v39, |v26|, |v27|
	v_max3_f32 v39, v39, |v28|, |v29|
	v_max3_f32 v34, v39, |v30|, |v31|
	v_max3_f32 v36, |v2|, 0, |v3|
	v_max3_f32 v36, v36, |v4|, |v5|
	v_max3_f32 v36, v36, |v6|, |v7|
	v_max3_f32 v36, v36, |v8|, |v9|
	v_max3_f32 v36, v36, |v10|, |v11|
	v_max3_f32 v36, v36, |v12|, |v13|
	v_max3_f32 v36, v36, |v14|, |v15|
	v_max3_f32 v34, v34, |v32|, |v33|
	v_max3_f32 v36, v36, |v16|, |v17|
	v_mov_b32_e32 v35, v34
	v_mov_b32_e32 v37, v36
	s_nop 0
	v_permlane32_swap_b32_e32 v34, v35
	v_permlane32_swap_b32_e32 v36, v37
	s_and_saveexec_b64 s[4:5], vcc
	s_cbranch_execz .LBB1_6
	v_max_f32_e32 v34, v34, v34
	v_max_f32_e32 v35, v35, v35
	v_max_f32_e32 v34, v34, v35
	v_and_b32_e32 v35, 0x1c0, v0
	v_max_f32_e32 v36, v36, v36
	v_max_f32_e32 v37, v37, v37
	v_lshl_add_u32 v35, v35, 2, v38
	v_max_f32_e32 v36, v36, v37
	v_add_u32_e32 v35, 0x8800, v35
	ds_write2_b32 v35, v34, v36 offset1:32
